# v8 + one w_down sjob per wave hosted in each gate_up epilogue (loads behind the bias loads, convert+store after the last epilogue store); streaming K-loop trips only in units 1-3
# speedup vs baseline: 1.0127x; 1.0127x over previous
;     __device__ __forceinline__ void operator()(const f32x4 (&acc)[2][2][4][2], const Unit& u, int wr, int wc, int fr, int fq) const {
;         const int row0 = u.pm * BM + wr * 64 + fr, cc = u.pn * HALF + wc * 32 + 8 * fq;
;         const float* bp = bias + (size_t)u.e * 4096 + cc;
;         f32x4 bg[2], bu[2];
; #pragma unroll
;         for (int n = 0; n < 2; ++n) { bg[n] = *(const f32x4*)(bp + 4 * n); bu[n] = *(const f32x4*)(bp + 2048 + 4 * n); }
; #pragma unroll
;         for (int ai = 0; ai < 2; ++ai)
; #pragma unroll
;             for (int m = 0; m < 4; ++m) { float r[8];
; #pragma unroll
;                 for (int n = 0; n < 2; ++n)
; #pragma unroll
;                     for (int j = 0; j < 4; ++j) {
;                         float g = acc[ai][0][m][n][j] * W8_INV + bg[n][j], uu = acc[ai][1][m][n][j] * W8_INV + bu[n][j];
;                         g = fminf(g, 7.0f); uu = fminf(fmaxf(uu, -7.0f), 7.0f);
;                         const float glu = g * __builtin_amdgcn_rcpf(1.0f + __expf(-1.702f * g));
;                         r[n * 4 + j] = (uu + 1.0f) * glu; }
;                 u32x2 w; w.x = pk4_fp8(r[0], r[1], r[2], r[3]); w.y = pk4_fp8(r[4], r[5], r[6], r[7]);
;                 *(u32x2*)(O + (size_t)(row0 + ai * HALF + m * 16) * DM + cc) = w; }
; __device__ __forceinline__ SJob sjob_addr(const Args& a, int j, int lane) {
;     SJob c; const int kseg = lane & 7, nq = lane >> 3;
;     if (j < SJOBS_GU) { const int e = j >> 12, kb = (j >> 7) & 31, nb = j & 127, s0 = nb * 32, bj = s0 >> 11, rem = s0 & 2047, pn = rem >> 7, c0 = rem & 127, np = pn * 256 + bj * 128 + c0;
;         c.ld = 4096; c.src = a.w_gate_up + ((size_t)e * 2048 + kb * 64 + kseg * 8) * 4096 + s0 + nq * 4; c.dst = (unsigned char*)(a.ws + WS_WGU_T) + ((size_t)e * 4096 + np + nq * 4) * 2048 + kb * 64 + kseg * 8; }
;     else { const int jj = j - SJOBS_GU, e = jj >> 11, kb = (jj >> 6) & 31, nb = jj & 63;
;         c.ld = 2048; c.src = a.w_down + ((size_t)e * 2048 + kb * 64 + kseg * 8) * 2048 + nb * 32 + nq * 4; c.dst = (unsigned char*)(a.ws + WS_WD_T) + ((size_t)e * 2048 + nb * 32 + nq * 4) * 2048 + kb * 64 + kseg * 8; }
;     return c;
; }
; __device__ __forceinline__ void sjob_load(const SJob& c, f32x4 (&v)[8]) {
; #pragma unroll
;     for (int r = 0; r < 8; ++r) v[r] = __builtin_nontemporal_load((const f32x4*)(c.src + (size_t)r * c.ld));
.LBB0_853:
	v_mov_b32_e32 v18, v0
	s_lshl_b32 s0, s36, 7
	v_lshrrev_b32_e32 v2, 1, v18
	s_ashr_i32 s35, s34, 31
	v_and_or_b32 v2, v2, 24, s0
	s_lshl_b64 s[0:1], s[34:35], 14
	v_or_b32_e32 v20, s77, v2
	s_add_u32 s0, s48, s0
	s_addc_u32 s1, s49, s1
	v_ashrrev_i32_e32 v21, 31, v20
	v_lshl_add_u64 v[2:3], v[20:21], 2, s[0:1]
	global_load_dwordx4 v[14:17], v[2:3], off
	global_load_dwordx4 v[6:9], v[2:3], off offset:16
	v_add_co_u32_e32 v4, vcc, s56, v2
	v_and_or_b32 v18, v18, 15, s76
	s_nop 0
	v_addc_co_u32_e32 v5, vcc, 0, v3, vcc
	v_lshl_add_u64 v[2:3], v[2:3], 0, s[14:15]
	global_load_dwordx4 v[10:13], v[4:5], off
	v_lshl_add_u32 v22, s24, 8, v18
	global_load_dwordx4 v[2:5], v[2:3], off offset:16
	s_mov_b32 s34, s16
	s_mov_b32 s36, s18
	s_mov_b32 s24, s81
	s_mov_b64 s[0:1], s[20:21]
	s_lshr_b32 s90, s98, 1
	s_mul_i32 s90, s90, s83
	s_add_i32 s90, s90, s84
	s_cmp_lt_u32 s90, 0x8000
	s_cbranch_scc0 .Lesj_no
	s_lshr_b32 s91, s90, 10
	s_lshl_b32 s91, s91, 11
	s_and_b32 s99, s90, 0x3c0
	s_lshl_b32 s99, s99, 1
	s_or_b32 s91, s91, s99
	s_and_b32 s99, s98, 1
	s_lshl_b32 s99, s99, 6
	s_or_b32 s91, s91, s99
	s_and_b32 s90, s90, 63
	s_or_b32 s90, s90, s91
	s_lshr_b32 s91, s90, 11
	s_and_b32 s99, s90, 0x7c0
	s_and_b32 s82, s90, 63
	s_lshl_b32 s32, s91, 24
	s_lshl_b32 s100, s99, 13
	s_add_i32 s32, s32, s100
	s_lshl_b32 s100, s82, 7
	s_add_i32 s32, s32, s100
	s_add_u32 s100, s86, s32
	s_addc_u32 s101, s87, 0
	s_lshl_b32 s32, s91, 22
	s_lshl_b32 s82, s82, 16
	s_add_i32 s32, s32, s82
	s_add_i32 s32, s32, s99
	s_add_u32 s90, s88, s32
	s_addc_u32 s91, s89, 0
	global_load_dwordx4 v[218:221], v252, s[100:101] nt
	s_add_u32 s100, s100, 0x2000
	s_addc_u32 s101, s101, 0
	global_load_dwordx4 v[222:225], v252, s[100:101] nt
	s_add_u32 s100, s100, 0x2000
	s_addc_u32 s101, s101, 0
	global_load_dwordx4 v[226:229], v252, s[100:101] nt
	s_add_u32 s100, s100, 0x2000
	s_addc_u32 s101, s101, 0
	global_load_dwordx4 v[230:233], v252, s[100:101] nt
	s_add_u32 s100, s100, 0x2000
	s_addc_u32 s101, s101, 0
	global_load_dwordx4 v[234:237], v252, s[100:101] nt
	s_add_u32 s100, s100, 0x2000
	s_addc_u32 s101, s101, 0
	global_load_dwordx4 v[238:241], v252, s[100:101] nt
	s_add_u32 s100, s100, 0x2000
	s_addc_u32 s101, s101, 0
	global_load_dwordx4 v[242:245], v252, s[100:101] nt
	s_add_u32 s100, s100, 0x2000
	s_addc_u32 s101, s101, 0
	global_load_dwordx4 v[246:249], v252, s[100:101] nt
	s_mov_b32 s82, 1
	s_waitcnt vmcnt(8)
	s_branch .Lesj_join
.Lesj_no:
	s_mov_b32 s82, 0
	s_waitcnt vmcnt(0)
.Lesj_join:
	v_fmamk_f32 v19, v175, 0x3c800000, v15
	v_fmamk_f32 v25, v166, 0x3c800000, v6
	v_min_f32_e32 v19, 0x40e00000, v19
	v_min_f32_e32 v25, 0x40e00000, v25
	v_fmamk_f32 v23, v176, 0x3c800000, v16
	v_mul_f32_e32 v36, 0xbfd9db23, v19
	v_mul_f32_e32 v39, 0xbfd9db23, v25
	v_min_f32_e32 v23, 0x40e00000, v23
	v_mul_f32_e32 v36, 0x3fb8aa3b, v36
	v_mul_f32_e32 v39, 0x3fb8aa3b, v39
	v_mul_f32_e32 v37, 0xbfd9db23, v23
	v_exp_f32_e32 v36, v36
	v_exp_f32_e32 v39, v39
	v_mul_f32_e32 v37, 0x3fb8aa3b, v37
	v_fmamk_f32 v18, v174, 0x3c800000, v14
	v_fmamk_f32 v24, v177, 0x3c800000, v17
	v_exp_f32_e32 v37, v37
	v_min_f32_e32 v18, 0x40e00000, v18
	v_min_f32_e32 v24, 0x40e00000, v24
	v_mul_f32_e32 v35, 0xbfd9db23, v18
	v_mul_f32_e32 v38, 0xbfd9db23, v24
	v_add_f32_e32 v36, 1.0, v36
	v_add_f32_e32 v39, 1.0, v39
	v_mul_f32_e32 v35, 0x3fb8aa3b, v35
	v_mul_f32_e32 v38, 0x3fb8aa3b, v38
	v_rcp_f32_e32 v36, v36
	v_rcp_f32_e32 v39, v39
	v_exp_f32_e32 v35, v35
	v_exp_f32_e32 v38, v38
	v_add_f32_e32 v37, 1.0, v37
	v_fmamk_f32 v27, v168, 0x3c800000, v8
	v_fmamk_f32 v29, v171, 0x3c800000, v11
	v_fmamk_f32 v32, v162, 0x3c800000, v2
	v_rcp_f32_e32 v37, v37
	v_min_f32_e32 v27, 0x40e00000, v27
	v_med3_f32 v29, v29, s57, v196
	v_med3_f32 v32, v32, s57, v196
	v_fmamk_f32 v26, v167, 0x3c800000, v7
	v_fmamk_f32 v30, v172, 0x3c800000, v12
	v_mul_f32_e32 v41, 0xbfd9db23, v27
	v_add_f32_e32 v29, 1.0, v29
	v_add_f32_e32 v32, 1.0, v32
	v_mul_f32_e32 v19, v19, v36
	v_mul_f32_e32 v25, v25, v39
	v_min_f32_e32 v26, 0x40e00000, v26
	v_med3_f32 v30, v30, s57, v196
	v_mul_f32_e32 v41, 0x3fb8aa3b, v41
	v_add_f32_e32 v35, 1.0, v35
	v_add_f32_e32 v38, 1.0, v38
	v_mul_f32_e32 v19, v29, v19
	v_mul_f32_e32 v29, v32, v25
	v_fmamk_f32 v25, v169, 0x3c800000, v9
	v_mul_f32_e32 v40, 0xbfd9db23, v26
	v_add_f32_e32 v30, 1.0, v30
	v_exp_f32_e32 v41, v41
	v_rcp_f32_e32 v35, v35
	v_rcp_f32_e32 v38, v38
	v_mul_f32_e32 v23, v23, v37
	v_min_f32_e32 v25, 0x40e00000, v25
	v_mul_f32_e32 v40, 0x3fb8aa3b, v40
	v_mul_f32_e32 v23, v30, v23
	v_mul_f32_e32 v30, 0xbfd9db23, v25
	v_fmamk_f32 v28, v170, 0x3c800000, v10
	v_fmamk_f32 v31, v173, 0x3c800000, v13
	v_exp_f32_e32 v40, v40
	v_mul_f32_e32 v30, 0x3fb8aa3b, v30
	v_med3_f32 v28, v28, s57, v196
	v_med3_f32 v31, v31, s57, v196
	v_exp_f32_e32 v30, v30
	v_add_f32_e32 v28, 1.0, v28
	v_add_f32_e32 v31, 1.0, v31
	v_add_f32_e32 v41, 1.0, v41
	v_mul_f32_e32 v18, v18, v35
	v_mul_f32_e32 v24, v24, v38
	v_mul_f32_e32 v18, v28, v18
	v_mul_f32_e32 v28, v31, v24
	v_rcp_f32_e32 v24, v41
	v_add_f32_e32 v40, 1.0, v40
	v_fmamk_f32 v34, v164, 0x3c800000, v4
	v_rcp_f32_e32 v40, v40
	v_add_f32_e32 v30, 1.0, v30
	v_med3_f32 v31, v34, s57, v196
	v_rcp_f32_e32 v30, v30
	v_fmamk_f32 v33, v163, 0x3c800000, v3
	v_mul_f32_e32 v24, v27, v24
	v_add_f32_e32 v27, 1.0, v31
	v_med3_f32 v33, v33, s57, v196
	v_mul_f32_e32 v27, v27, v24
	v_fmamk_f32 v24, v165, 0x3c800000, v5
	v_add_f32_e32 v33, 1.0, v33
	v_mul_f32_e32 v26, v26, v40
	v_med3_f32 v31, v24, s57, v196
	v_mov_b32_e32 v24, v181
	v_mul_f32_e32 v26, v33, v26
	v_mul_f32_e32 v30, v25, v30
	v_cvt_pk_fp8_f32 v24, v18, v19
	v_mov_b32_e32 v25, v181
	v_cvt_pk_fp8_f32 v25, v29, v26
	v_add_f32_e32 v18, 1.0, v31
; __device__ __forceinline__ unsigned pk4_fp8(float a, float b, float c, float d) { int p = __builtin_amdgcn_cvt_pk_fp8_f32(a, b, 0, false); p = __builtin_amdgcn_cvt_pk_fp8_f32(c, d, p, true); return (unsigned)p; }
;     __device__ __forceinline__ void operator()(const f32x4 (&acc)[2][2][4][2], const Unit& u, int wr, int wc, int fr, int fq) const {
;     ...
;             for (int m = 0; m < 4; ++m) { float r[8];
; #pragma unroll
;                 for (int n = 0; n < 2; ++n)
; #pragma unroll
;                     for (int j = 0; j < 4; ++j) {
;                         float g = acc[ai][0][m][n][j] * W8_INV + bg[n][j], uu = acc[ai][1][m][n][j] * W8_INV + bu[n][j];
;                         g = fminf(g, 7.0f); uu = fminf(fmaxf(uu, -7.0f), 7.0f);
;                         const float glu = g * __builtin_amdgcn_rcpf(1.0f + __expf(-1.702f * g));
;                         r[n * 4 + j] = (uu + 1.0f) * glu; }
;                 u32x2 w; w.x = pk4_fp8(r[0], r[1], r[2], r[3]); w.y = pk4_fp8(r[4], r[5], r[6], r[7]);
;                 *(u32x2*)(O + (size_t)(row0 + ai * HALF + m * 16) * DM + cc) = w; }
	v_mul_f32_e32 v18, v18, v30
	v_cvt_pk_fp8_f32 v24, v23, v28 op_sel:[0,0,1]
	v_ashrrev_i32_e32 v23, 31, v22
	v_cvt_pk_fp8_f32 v25, v27, v18 op_sel:[0,0,1]
	v_lshlrev_b64 v[18:19], 11, v[22:23]
	v_fmamk_f32 v23, v158, 0x3c800000, v14
	v_min_f32_e32 v23, 0x40e00000, v23
	v_mul_f32_e32 v26, 0xbfd9db23, v23
	v_mul_f32_e32 v26, 0x3fb8aa3b, v26
	v_exp_f32_e32 v26, v26
	v_lshl_add_u64 v[18:19], s[8:9], 0, v[18:19]
	v_lshl_add_u64 v[18:19], v[18:19], 0, v[20:21]
	global_store_dwordx2 v[18:19], v[24:25], off
	v_add_f32_e32 v25, 1.0, v26
	v_fmamk_f32 v26, v159, 0x3c800000, v15
	v_min_f32_e32 v26, 0x40e00000, v26
	v_mul_f32_e32 v27, 0xbfd9db23, v26
	v_mul_f32_e32 v27, 0x3fb8aa3b, v27
	v_rcp_f32_e32 v25, v25
	v_exp_f32_e32 v27, v27
	v_fmamk_f32 v28, v161, 0x3c800000, v17
	v_min_f32_e32 v28, 0x40e00000, v28
	v_mul_f32_e32 v23, v23, v25
	v_add_f32_e32 v25, 1.0, v27
	v_rcp_f32_e32 v25, v25
	v_mul_f32_e32 v29, 0xbfd9db23, v28
	v_mul_f32_e32 v29, 0x3fb8aa3b, v29
	v_exp_f32_e32 v29, v29
	v_mul_f32_e32 v25, v26, v25
	v_fmamk_f32 v26, v160, 0x3c800000, v16
	v_min_f32_e32 v26, 0x40e00000, v26
	v_mul_f32_e32 v27, 0xbfd9db23, v26
	v_mul_f32_e32 v27, 0x3fb8aa3b, v27
	v_exp_f32_e32 v27, v27
	v_fmamk_f32 v30, v151, 0x3c800000, v7
	v_min_f32_e32 v30, 0x40e00000, v30
	v_mul_f32_e32 v31, 0xbfd9db23, v30
	v_add_f32_e32 v27, 1.0, v27
	v_rcp_f32_e32 v27, v27
	v_mul_f32_e32 v31, 0x3fb8aa3b, v31
	v_exp_f32_e32 v31, v31
	v_fmamk_f32 v24, v154, 0x3c800000, v10
	v_mul_f32_e32 v26, v26, v27
	v_add_f32_e32 v27, 1.0, v29
	v_rcp_f32_e32 v27, v27
	v_med3_f32 v24, v24, s57, v196
	v_add_f32_e32 v24, 1.0, v24
	v_mul_f32_e32 v23, v24, v23
	v_mul_f32_e32 v27, v28, v27
	v_fmamk_f32 v28, v150, 0x3c800000, v6
	v_min_f32_e32 v28, 0x40e00000, v28
	v_mul_f32_e32 v29, 0xbfd9db23, v28
	v_mul_f32_e32 v29, 0x3fb8aa3b, v29
	v_exp_f32_e32 v29, v29
	v_fmamk_f32 v24, v155, 0x3c800000, v11
	v_med3_f32 v24, v24, s57, v196
	v_add_f32_e32 v24, 1.0, v24
	v_add_f32_e32 v29, 1.0, v29
	v_rcp_f32_e32 v29, v29
	v_mul_f32_e32 v25, v24, v25
	v_fmamk_f32 v24, v156, 0x3c800000, v12
	v_med3_f32 v24, v24, s57, v196
	v_mul_f32_e32 v28, v28, v29
	v_add_f32_e32 v29, 1.0, v31
	v_rcp_f32_e32 v29, v29
	v_add_f32_e32 v24, 1.0, v24
	v_mul_f32_e32 v26, v24, v26
	v_fmamk_f32 v24, v157, 0x3c800000, v13
	v_mul_f32_e32 v29, v30, v29
	v_fmamk_f32 v30, v152, 0x3c800000, v8
	v_min_f32_e32 v30, 0x40e00000, v30
	v_mul_f32_e32 v31, 0xbfd9db23, v30
	v_med3_f32 v24, v24, s57, v196
	v_mul_f32_e32 v31, 0x3fb8aa3b, v31
	v_add_f32_e32 v24, 1.0, v24
	v_exp_f32_e32 v31, v31
	v_mul_f32_e32 v27, v24, v27
	v_fmamk_f32 v24, v146, 0x3c800000, v2
	v_med3_f32 v24, v24, s57, v196
	v_fmamk_f32 v32, v153, 0x3c800000, v9
	v_add_f32_e32 v24, 1.0, v24
	v_min_f32_e32 v32, 0x40e00000, v32
	v_mul_f32_e32 v28, v24, v28
	v_fmamk_f32 v24, v147, 0x3c800000, v3
	v_add_f32_e32 v31, 1.0, v31
	v_mul_f32_e32 v33, 0xbfd9db23, v32
	v_med3_f32 v24, v24, s57, v196
	v_rcp_f32_e32 v31, v31
	v_mul_f32_e32 v33, 0x3fb8aa3b, v33
	v_add_f32_e32 v24, 1.0, v24
	v_exp_f32_e32 v33, v33
	v_mul_f32_e32 v29, v24, v29
	v_fmamk_f32 v24, v148, 0x3c800000, v4
	v_med3_f32 v24, v24, s57, v196
	v_mul_f32_e32 v30, v30, v31
	v_add_f32_e32 v24, 1.0, v24
	v_add_f32_e32 v31, 1.0, v33
	v_mul_f32_e32 v30, v24, v30
	v_fmamk_f32 v24, v149, 0x3c800000, v5
	v_rcp_f32_e32 v31, v31
	v_med3_f32 v33, v24, s57, v196
	v_mov_b32_e32 v24, v181
	v_cvt_pk_fp8_f32 v24, v23, v25
	v_mov_b32_e32 v25, v181
	v_cvt_pk_fp8_f32 v25, v28, v29
	v_mul_f32_e32 v31, v32, v31
	v_add_f32_e32 v23, 1.0, v33
	v_mul_f32_e32 v23, v23, v31
	v_cvt_pk_fp8_f32 v24, v26, v27 op_sel:[0,0,1]
	v_cvt_pk_fp8_f32 v25, v30, v23 op_sel:[0,0,1]
	v_or_b32_e32 v26, 16, v22
	v_fmamk_f32 v23, v142, 0x3c800000, v14
	v_ashrrev_i32_e32 v27, 31, v26
	v_min_f32_e32 v23, 0x40e00000, v23
	v_lshlrev_b64 v[26:27], 11, v[26:27]
	v_mul_f32_e32 v28, 0xbfd9db23, v23
	v_lshl_add_u64 v[26:27], s[8:9], 0, v[26:27]
	v_mul_f32_e32 v28, 0x3fb8aa3b, v28
	v_exp_f32_e32 v28, v28
	v_lshl_add_u64 v[26:27], v[26:27], 0, v[20:21]
	global_store_dwordx2 v[26:27], v[24:25], off
	v_fmamk_f32 v26, v143, 0x3c800000, v15
	v_min_f32_e32 v26, 0x40e00000, v26
	v_mul_f32_e32 v27, 0xbfd9db23, v26
	v_add_f32_e32 v25, 1.0, v28
	v_mul_f32_e32 v27, 0x3fb8aa3b, v27
	v_rcp_f32_e32 v25, v25
	v_exp_f32_e32 v27, v27
	v_fmamk_f32 v28, v145, 0x3c800000, v17
	v_min_f32_e32 v28, 0x40e00000, v28
	v_mul_f32_e32 v23, v23, v25
	v_add_f32_e32 v25, 1.0, v27
	v_rcp_f32_e32 v25, v25
	v_mul_f32_e32 v29, 0xbfd9db23, v28
	v_mul_f32_e32 v29, 0x3fb8aa3b, v29
	v_exp_f32_e32 v29, v29
	v_mul_f32_e32 v25, v26, v25
	v_fmamk_f32 v26, v144, 0x3c800000, v16
	v_min_f32_e32 v26, 0x40e00000, v26
	v_mul_f32_e32 v27, 0xbfd9db23, v26
	v_mul_f32_e32 v27, 0x3fb8aa3b, v27
	v_exp_f32_e32 v27, v27
	v_fmamk_f32 v30, v135, 0x3c800000, v7
	v_min_f32_e32 v30, 0x40e00000, v30
	v_mul_f32_e32 v31, 0xbfd9db23, v30
	v_add_f32_e32 v27, 1.0, v27
	v_rcp_f32_e32 v27, v27
	v_mul_f32_e32 v31, 0x3fb8aa3b, v31
	v_exp_f32_e32 v31, v31
	v_fmamk_f32 v24, v138, 0x3c800000, v10
	v_mul_f32_e32 v26, v26, v27
	v_add_f32_e32 v27, 1.0, v29
	v_rcp_f32_e32 v27, v27
	v_med3_f32 v24, v24, s57, v196
	v_add_f32_e32 v24, 1.0, v24
	v_mul_f32_e32 v23, v24, v23
	v_mul_f32_e32 v27, v28, v27
	v_fmamk_f32 v28, v134, 0x3c800000, v6
	v_min_f32_e32 v28, 0x40e00000, v28
	v_mul_f32_e32 v29, 0xbfd9db23, v28
	v_mul_f32_e32 v29, 0x3fb8aa3b, v29
	v_exp_f32_e32 v29, v29
	v_fmamk_f32 v24, v139, 0x3c800000, v11
	v_med3_f32 v24, v24, s57, v196
	v_add_f32_e32 v24, 1.0, v24
	v_add_f32_e32 v29, 1.0, v29
	v_rcp_f32_e32 v29, v29
	v_mul_f32_e32 v25, v24, v25
	v_fmamk_f32 v24, v140, 0x3c800000, v12
	v_med3_f32 v24, v24, s57, v196
	v_mul_f32_e32 v28, v28, v29
	v_add_f32_e32 v29, 1.0, v31
; __device__ __forceinline__ unsigned pk4_fp8(float a, float b, float c, float d) { int p = __builtin_amdgcn_cvt_pk_fp8_f32(a, b, 0, false); p = __builtin_amdgcn_cvt_pk_fp8_f32(c, d, p, true); return (unsigned)p; }
;     __device__ __forceinline__ void operator()(const f32x4 (&acc)[2][2][4][2], const Unit& u, int wr, int wc, int fr, int fq) const {
;     ...
;             for (int m = 0; m < 4; ++m) { float r[8];
; #pragma unroll
;                 for (int n = 0; n < 2; ++n)
; #pragma unroll
;                     for (int j = 0; j < 4; ++j) {
;                         float g = acc[ai][0][m][n][j] * W8_INV + bg[n][j], uu = acc[ai][1][m][n][j] * W8_INV + bu[n][j];
;                         g = fminf(g, 7.0f); uu = fminf(fmaxf(uu, -7.0f), 7.0f);
;                         const float glu = g * __builtin_amdgcn_rcpf(1.0f + __expf(-1.702f * g));
;                         r[n * 4 + j] = (uu + 1.0f) * glu; }
;                 u32x2 w; w.x = pk4_fp8(r[0], r[1], r[2], r[3]); w.y = pk4_fp8(r[4], r[5], r[6], r[7]);
;                 *(u32x2*)(O + (size_t)(row0 + ai * HALF + m * 16) * DM + cc) = w; }
	v_rcp_f32_e32 v29, v29
	v_add_f32_e32 v24, 1.0, v24
	v_mul_f32_e32 v26, v24, v26
	v_fmamk_f32 v24, v141, 0x3c800000, v13
	v_mul_f32_e32 v29, v30, v29
	v_fmamk_f32 v30, v136, 0x3c800000, v8
	v_min_f32_e32 v30, 0x40e00000, v30
	v_mul_f32_e32 v31, 0xbfd9db23, v30
	v_med3_f32 v24, v24, s57, v196
	v_mul_f32_e32 v31, 0x3fb8aa3b, v31
	v_add_f32_e32 v24, 1.0, v24
	v_exp_f32_e32 v31, v31
	v_mul_f32_e32 v27, v24, v27
	v_fmamk_f32 v24, v130, 0x3c800000, v2
	v_med3_f32 v24, v24, s57, v196
	v_fmamk_f32 v32, v137, 0x3c800000, v9
	v_add_f32_e32 v24, 1.0, v24
	v_min_f32_e32 v32, 0x40e00000, v32
	v_mul_f32_e32 v28, v24, v28
	v_fmamk_f32 v24, v131, 0x3c800000, v3
	v_add_f32_e32 v31, 1.0, v31
	v_mul_f32_e32 v33, 0xbfd9db23, v32
	v_med3_f32 v24, v24, s57, v196
	v_rcp_f32_e32 v31, v31
	v_mul_f32_e32 v33, 0x3fb8aa3b, v33
	v_add_f32_e32 v24, 1.0, v24
	v_exp_f32_e32 v33, v33
	v_mul_f32_e32 v29, v24, v29
	v_fmamk_f32 v24, v132, 0x3c800000, v4
	v_med3_f32 v24, v24, s57, v196
	v_mul_f32_e32 v30, v30, v31
	v_add_f32_e32 v24, 1.0, v24
	v_add_f32_e32 v31, 1.0, v33
	v_mul_f32_e32 v30, v24, v30
	v_fmamk_f32 v24, v133, 0x3c800000, v5
	v_rcp_f32_e32 v31, v31
	v_med3_f32 v33, v24, s57, v196
	v_mov_b32_e32 v24, v181
	v_cvt_pk_fp8_f32 v24, v23, v25
	v_mov_b32_e32 v25, v181
	v_cvt_pk_fp8_f32 v25, v28, v29
	v_mul_f32_e32 v31, v32, v31
	v_add_f32_e32 v23, 1.0, v33
	v_mul_f32_e32 v23, v23, v31
	v_cvt_pk_fp8_f32 v24, v26, v27 op_sel:[0,0,1]
	v_cvt_pk_fp8_f32 v25, v30, v23 op_sel:[0,0,1]
	v_or_b32_e32 v26, 32, v22
	v_fmamk_f32 v23, v126, 0x3c800000, v14
	v_ashrrev_i32_e32 v27, 31, v26
	v_min_f32_e32 v23, 0x40e00000, v23
	v_lshlrev_b64 v[26:27], 11, v[26:27]
	v_mul_f32_e32 v28, 0xbfd9db23, v23
	v_lshl_add_u64 v[26:27], s[8:9], 0, v[26:27]
	v_mul_f32_e32 v28, 0x3fb8aa3b, v28
	v_exp_f32_e32 v28, v28
	v_lshl_add_u64 v[26:27], v[26:27], 0, v[20:21]
	global_store_dwordx2 v[26:27], v[24:25], off
	v_fmamk_f32 v26, v127, 0x3c800000, v15
	v_min_f32_e32 v26, 0x40e00000, v26
	v_mul_f32_e32 v27, 0xbfd9db23, v26
	v_add_f32_e32 v25, 1.0, v28
	v_mul_f32_e32 v27, 0x3fb8aa3b, v27
	v_rcp_f32_e32 v25, v25
	v_exp_f32_e32 v27, v27
	v_fmamk_f32 v28, v129, 0x3c800000, v17
	v_min_f32_e32 v28, 0x40e00000, v28
	v_mul_f32_e32 v23, v23, v25
	v_add_f32_e32 v25, 1.0, v27
	v_rcp_f32_e32 v25, v25
	v_mul_f32_e32 v29, 0xbfd9db23, v28
	v_mul_f32_e32 v29, 0x3fb8aa3b, v29
	v_exp_f32_e32 v29, v29
	v_mul_f32_e32 v25, v26, v25
	v_fmamk_f32 v26, v128, 0x3c800000, v16
	v_min_f32_e32 v26, 0x40e00000, v26
	v_mul_f32_e32 v27, 0xbfd9db23, v26
	v_mul_f32_e32 v27, 0x3fb8aa3b, v27
	v_exp_f32_e32 v27, v27
	v_fmamk_f32 v30, v119, 0x3c800000, v7
	v_min_f32_e32 v30, 0x40e00000, v30
	v_mul_f32_e32 v31, 0xbfd9db23, v30
	v_add_f32_e32 v27, 1.0, v27
	v_rcp_f32_e32 v27, v27
	v_mul_f32_e32 v31, 0x3fb8aa3b, v31
	v_exp_f32_e32 v31, v31
	v_fmamk_f32 v24, v122, 0x3c800000, v10
	v_mul_f32_e32 v26, v26, v27
	v_add_f32_e32 v27, 1.0, v29
	v_rcp_f32_e32 v27, v27
	v_med3_f32 v24, v24, s57, v196
	v_add_f32_e32 v24, 1.0, v24
	v_mul_f32_e32 v23, v24, v23
	v_mul_f32_e32 v27, v28, v27
	v_fmamk_f32 v28, v118, 0x3c800000, v6
	v_min_f32_e32 v28, 0x40e00000, v28
	v_mul_f32_e32 v29, 0xbfd9db23, v28
	v_mul_f32_e32 v29, 0x3fb8aa3b, v29
	v_exp_f32_e32 v29, v29
	v_fmamk_f32 v24, v123, 0x3c800000, v11
	v_med3_f32 v24, v24, s57, v196
	v_add_f32_e32 v24, 1.0, v24
	v_add_f32_e32 v29, 1.0, v29
	v_rcp_f32_e32 v29, v29
	v_mul_f32_e32 v25, v24, v25
	v_fmamk_f32 v24, v124, 0x3c800000, v12
	v_med3_f32 v24, v24, s57, v196
	v_mul_f32_e32 v28, v28, v29
	v_add_f32_e32 v29, 1.0, v31
	v_rcp_f32_e32 v29, v29
	v_add_f32_e32 v24, 1.0, v24
	v_mul_f32_e32 v26, v24, v26
	v_fmamk_f32 v24, v125, 0x3c800000, v13
	v_mul_f32_e32 v29, v30, v29
	v_fmamk_f32 v30, v120, 0x3c800000, v8
	v_min_f32_e32 v30, 0x40e00000, v30
	v_mul_f32_e32 v31, 0xbfd9db23, v30
	v_med3_f32 v24, v24, s57, v196
	v_mul_f32_e32 v31, 0x3fb8aa3b, v31
	v_add_f32_e32 v24, 1.0, v24
	v_exp_f32_e32 v31, v31
	v_mul_f32_e32 v27, v24, v27
	v_fmamk_f32 v24, v114, 0x3c800000, v2
	v_med3_f32 v24, v24, s57, v196
	v_fmamk_f32 v32, v121, 0x3c800000, v9
	v_add_f32_e32 v24, 1.0, v24
	v_min_f32_e32 v32, 0x40e00000, v32
	v_mul_f32_e32 v28, v24, v28
	v_fmamk_f32 v24, v115, 0x3c800000, v3
	v_add_f32_e32 v31, 1.0, v31
	v_mul_f32_e32 v33, 0xbfd9db23, v32
	v_med3_f32 v24, v24, s57, v196
	v_rcp_f32_e32 v31, v31
	v_mul_f32_e32 v33, 0x3fb8aa3b, v33
	v_add_f32_e32 v24, 1.0, v24
	v_exp_f32_e32 v33, v33
	v_mul_f32_e32 v29, v24, v29
	v_fmamk_f32 v24, v116, 0x3c800000, v4
	v_med3_f32 v24, v24, s57, v196
	v_mul_f32_e32 v30, v30, v31
	v_add_f32_e32 v24, 1.0, v24
	v_add_f32_e32 v31, 1.0, v33
	v_mul_f32_e32 v30, v24, v30
	v_fmamk_f32 v24, v117, 0x3c800000, v5
	v_rcp_f32_e32 v31, v31
	v_med3_f32 v33, v24, s57, v196
	v_mov_b32_e32 v24, v181
	v_cvt_pk_fp8_f32 v24, v23, v25
	v_mov_b32_e32 v25, v181
	v_cvt_pk_fp8_f32 v25, v28, v29
	v_mul_f32_e32 v31, v32, v31
	v_add_f32_e32 v23, 1.0, v33
	v_mul_f32_e32 v23, v23, v31
	v_or_b32_e32 v22, 48, v22
	v_cvt_pk_fp8_f32 v25, v30, v23 op_sel:[0,0,1]
	v_ashrrev_i32_e32 v23, 31, v22
	v_lshlrev_b64 v[22:23], 11, v[22:23]
	v_lshl_add_u64 v[22:23], s[8:9], 0, v[22:23]
	v_lshl_add_u64 v[20:21], v[22:23], 0, v[20:21]
	v_fmamk_f32 v22, v111, 0x3c800000, v15
	v_min_f32_e32 v22, 0x40e00000, v22
	v_mul_f32_e32 v23, 0xbfd9db23, v22
	v_mul_f32_e32 v23, 0x3fb8aa3b, v23
	v_exp_f32_e32 v23, v23
	v_cvt_pk_fp8_f32 v24, v26, v27 op_sel:[0,0,1]
	v_fmamk_f32 v26, v110, 0x3c800000, v14
	v_min_f32_e32 v26, 0x40e00000, v26
	v_add_f32_e32 v23, 1.0, v23
	v_mul_f32_e32 v27, 0xbfd9db23, v26
	v_rcp_f32_e32 v23, v23
	v_mul_f32_e32 v27, 0x3fb8aa3b, v27
	v_exp_f32_e32 v27, v27
	global_store_dwordx2 v[20:21], v[24:25], off
	v_mul_f32_e32 v22, v22, v23
; __device__ __forceinline__ unsigned pk4_fp8(float a, float b, float c, float d) { int p = __builtin_amdgcn_cvt_pk_fp8_f32(a, b, 0, false); p = __builtin_amdgcn_cvt_pk_fp8_f32(c, d, p, true); return (unsigned)p; }
;     __device__ __forceinline__ void operator()(const f32x4 (&acc)[2][2][4][2], const Unit& u, int wr, int wc, int fr, int fq) const {
;     ...
;             for (int m = 0; m < 4; ++m) { float r[8];
; #pragma unroll
;                 for (int n = 0; n < 2; ++n)
; #pragma unroll
;                     for (int j = 0; j < 4; ++j) {
;                         float g = acc[ai][0][m][n][j] * W8_INV + bg[n][j], uu = acc[ai][1][m][n][j] * W8_INV + bu[n][j];
;                         g = fminf(g, 7.0f); uu = fminf(fmaxf(uu, -7.0f), 7.0f);
;                         const float glu = g * __builtin_amdgcn_rcpf(1.0f + __expf(-1.702f * g));
;                         r[n * 4 + j] = (uu + 1.0f) * glu; }
;                 u32x2 w; w.x = pk4_fp8(r[0], r[1], r[2], r[3]); w.y = pk4_fp8(r[4], r[5], r[6], r[7]);
;                 *(u32x2*)(O + (size_t)(row0 + ai * HALF + m * 16) * DM + cc) = w; }
	v_fmamk_f32 v23, v112, 0x3c800000, v16
	v_min_f32_e32 v23, 0x40e00000, v23
	v_add_f32_e32 v21, 1.0, v27
	v_mul_f32_e32 v24, 0xbfd9db23, v23
	v_rcp_f32_e32 v21, v21
	v_mul_f32_e32 v24, 0x3fb8aa3b, v24
	v_exp_f32_e32 v24, v24
	v_fmamk_f32 v25, v113, 0x3c800000, v17
	v_min_f32_e32 v25, 0x40e00000, v25
	v_mul_f32_e32 v21, v26, v21
	v_mul_f32_e32 v26, 0xbfd9db23, v25
	v_add_f32_e32 v24, 1.0, v24
	v_mul_f32_e32 v26, 0x3fb8aa3b, v26
	v_rcp_f32_e32 v24, v24
	v_exp_f32_e32 v26, v26
	v_fmamk_f32 v27, v103, 0x3c800000, v7
	v_min_f32_e32 v27, 0x40e00000, v27
	v_mul_f32_e32 v23, v23, v24
	v_add_f32_e32 v24, 1.0, v26
	v_rcp_f32_e32 v24, v24
	v_mul_f32_e32 v28, 0xbfd9db23, v27
	v_mul_f32_e32 v28, 0x3fb8aa3b, v28
	v_exp_f32_e32 v28, v28
	v_mul_f32_e32 v24, v25, v24
	v_fmamk_f32 v25, v102, 0x3c800000, v6
	v_min_f32_e32 v25, 0x40e00000, v25
	v_mul_f32_e32 v26, 0xbfd9db23, v25
	v_mul_f32_e32 v26, 0x3fb8aa3b, v26
	v_exp_f32_e32 v26, v26
	v_fmamk_f32 v20, v106, 0x3c800000, v10
	v_med3_f32 v20, v20, s57, v196
	v_add_f32_e32 v20, 1.0, v20
	v_add_f32_e32 v26, 1.0, v26
	v_rcp_f32_e32 v26, v26
	v_mul_f32_e32 v21, v20, v21
	v_fmamk_f32 v20, v107, 0x3c800000, v11
	v_med3_f32 v20, v20, s57, v196
	v_mul_f32_e32 v25, v25, v26
	v_add_f32_e32 v26, 1.0, v28
	v_rcp_f32_e32 v26, v26
	v_add_f32_e32 v20, 1.0, v20
	v_mul_f32_e32 v22, v20, v22
	v_fmamk_f32 v20, v108, 0x3c800000, v12
	v_med3_f32 v20, v20, s57, v196
	v_mul_f32_e32 v26, v27, v26
	v_fmamk_f32 v27, v104, 0x3c800000, v8
	v_add_f32_e32 v20, 1.0, v20
	v_min_f32_e32 v27, 0x40e00000, v27
	v_mul_f32_e32 v23, v20, v23
	v_fmamk_f32 v20, v109, 0x3c800000, v13
	v_mul_f32_e32 v28, 0xbfd9db23, v27
	v_med3_f32 v20, v20, s57, v196
	v_mul_f32_e32 v28, 0x3fb8aa3b, v28
	v_add_f32_e32 v20, 1.0, v20
	v_exp_f32_e32 v28, v28
	v_mul_f32_e32 v24, v20, v24
	v_fmamk_f32 v20, v98, 0x3c800000, v2
	v_med3_f32 v20, v20, s57, v196
	v_fmamk_f32 v29, v105, 0x3c800000, v9
	v_add_f32_e32 v20, 1.0, v20
	v_min_f32_e32 v29, 0x40e00000, v29
	v_mul_f32_e32 v25, v20, v25
	v_fmamk_f32 v20, v99, 0x3c800000, v3
	v_add_f32_e32 v28, 1.0, v28
	v_mul_f32_e32 v30, 0xbfd9db23, v29
	v_med3_f32 v20, v20, s57, v196
	v_rcp_f32_e32 v28, v28
	v_mul_f32_e32 v30, 0x3fb8aa3b, v30
	v_add_f32_e32 v20, 1.0, v20
	v_exp_f32_e32 v30, v30
	v_mul_f32_e32 v26, v20, v26
	v_fmamk_f32 v20, v100, 0x3c800000, v4
	v_med3_f32 v20, v20, s57, v196
	v_mul_f32_e32 v27, v27, v28
	v_add_f32_e32 v20, 1.0, v20
	v_add_f32_e32 v28, 1.0, v30
	v_mul_f32_e32 v27, v20, v27
	v_fmamk_f32 v20, v101, 0x3c800000, v5
	v_rcp_f32_e32 v28, v28
	v_med3_f32 v30, v20, s57, v196
	v_mov_b32_e32 v20, v181
	v_cvt_pk_fp8_f32 v20, v21, v22
	v_mov_b32_e32 v21, v181
	v_cvt_pk_fp8_f32 v21, v25, v26
	v_mul_f32_e32 v28, v29, v28
	v_add_f32_e32 v22, 1.0, v30
	v_mul_f32_e32 v22, v22, v28
	v_cvt_pk_fp8_f32 v21, v27, v22 op_sel:[0,0,1]
	v_fmamk_f32 v22, v94, 0x3c800000, v14
	v_cvt_pk_fp8_f32 v20, v23, v24 op_sel:[0,0,1]
	v_min_f32_e32 v24, 0x40e00000, v22
	v_mul_f32_e32 v22, 0xbfd9db23, v24
	v_mul_f32_e32 v22, 0x3fb8aa3b, v22
	v_exp_f32_e32 v25, v22
	v_add_co_u32_e32 v22, vcc, s58, v18
	v_fmamk_f32 v27, v87, 0x3c800000, v7
	s_nop 0
	v_addc_co_u32_e32 v23, vcc, 0, v19, vcc
	global_store_dwordx2 v[22:23], v[20:21], off
	v_fmamk_f32 v22, v95, 0x3c800000, v15
	v_min_f32_e32 v22, 0x40e00000, v22
	v_mul_f32_e32 v23, 0xbfd9db23, v22
	v_mul_f32_e32 v23, 0x3fb8aa3b, v23
	v_exp_f32_e32 v23, v23
	v_add_f32_e32 v21, 1.0, v25
	v_rcp_f32_e32 v21, v21
	v_fmamk_f32 v25, v97, 0x3c800000, v17
	v_add_f32_e32 v23, 1.0, v23
	v_rcp_f32_e32 v23, v23
	v_mul_f32_e32 v21, v24, v21
	v_min_f32_e32 v25, 0x40e00000, v25
	v_mul_f32_e32 v26, 0xbfd9db23, v25
	v_mul_f32_e32 v22, v22, v23
	v_fmamk_f32 v23, v96, 0x3c800000, v16
	v_min_f32_e32 v23, 0x40e00000, v23
	v_mul_f32_e32 v24, 0xbfd9db23, v23
	v_mul_f32_e32 v24, 0x3fb8aa3b, v24
	v_exp_f32_e32 v24, v24
	v_mul_f32_e32 v26, 0x3fb8aa3b, v26
	v_exp_f32_e32 v26, v26
	v_min_f32_e32 v27, 0x40e00000, v27
	v_add_f32_e32 v24, 1.0, v24
	v_rcp_f32_e32 v24, v24
	v_mul_f32_e32 v28, 0xbfd9db23, v27
	v_mul_f32_e32 v28, 0x3fb8aa3b, v28
	v_exp_f32_e32 v28, v28
	v_mul_f32_e32 v23, v23, v24
	v_add_f32_e32 v24, 1.0, v26
	v_rcp_f32_e32 v24, v24
	v_fmamk_f32 v20, v90, 0x3c800000, v10
	v_med3_f32 v20, v20, s57, v196
	v_add_f32_e32 v20, 1.0, v20
	v_mul_f32_e32 v24, v25, v24
	v_fmamk_f32 v25, v86, 0x3c800000, v6
	v_min_f32_e32 v25, 0x40e00000, v25
	v_mul_f32_e32 v26, 0xbfd9db23, v25
	v_mul_f32_e32 v26, 0x3fb8aa3b, v26
	v_exp_f32_e32 v26, v26
	v_mul_f32_e32 v21, v20, v21
	v_fmamk_f32 v20, v91, 0x3c800000, v11
	v_med3_f32 v20, v20, s57, v196
	v_add_f32_e32 v26, 1.0, v26
	v_rcp_f32_e32 v26, v26
	v_add_f32_e32 v20, 1.0, v20
	v_mul_f32_e32 v22, v20, v22
	v_fmamk_f32 v20, v92, 0x3c800000, v12
	v_mul_f32_e32 v25, v25, v26
	v_add_f32_e32 v26, 1.0, v28
	v_rcp_f32_e32 v26, v26
	v_med3_f32 v20, v20, s57, v196
	v_add_f32_e32 v20, 1.0, v20
	v_mul_f32_e32 v23, v20, v23
	v_mul_f32_e32 v26, v27, v26
	v_fmamk_f32 v27, v88, 0x3c800000, v8
	v_min_f32_e32 v27, 0x40e00000, v27
	v_fmamk_f32 v20, v93, 0x3c800000, v13
	v_mul_f32_e32 v28, 0xbfd9db23, v27
	v_med3_f32 v20, v20, s57, v196
	v_mul_f32_e32 v28, 0x3fb8aa3b, v28
	v_add_f32_e32 v20, 1.0, v20
	v_exp_f32_e32 v28, v28
	v_mul_f32_e32 v24, v20, v24
	v_fmamk_f32 v20, v82, 0x3c800000, v2
	v_med3_f32 v20, v20, s57, v196
	v_fmamk_f32 v29, v89, 0x3c800000, v9
	v_add_f32_e32 v20, 1.0, v20
	v_min_f32_e32 v29, 0x40e00000, v29
	v_mul_f32_e32 v25, v20, v25
	v_fmamk_f32 v20, v83, 0x3c800000, v3
	v_add_f32_e32 v28, 1.0, v28
	v_mul_f32_e32 v30, 0xbfd9db23, v29
	v_med3_f32 v20, v20, s57, v196
	v_rcp_f32_e32 v28, v28
	v_mul_f32_e32 v30, 0x3fb8aa3b, v30
	v_add_f32_e32 v20, 1.0, v20
	v_exp_f32_e32 v30, v30
; __device__ __forceinline__ unsigned pk4_fp8(float a, float b, float c, float d) { int p = __builtin_amdgcn_cvt_pk_fp8_f32(a, b, 0, false); p = __builtin_amdgcn_cvt_pk_fp8_f32(c, d, p, true); return (unsigned)p; }
;     __device__ __forceinline__ void operator()(const f32x4 (&acc)[2][2][4][2], const Unit& u, int wr, int wc, int fr, int fq) const {
;     ...
;             for (int m = 0; m < 4; ++m) { float r[8];
; #pragma unroll
;                 for (int n = 0; n < 2; ++n)
; #pragma unroll
;                     for (int j = 0; j < 4; ++j) {
;                         float g = acc[ai][0][m][n][j] * W8_INV + bg[n][j], uu = acc[ai][1][m][n][j] * W8_INV + bu[n][j];
;                         g = fminf(g, 7.0f); uu = fminf(fmaxf(uu, -7.0f), 7.0f);
;                         const float glu = g * __builtin_amdgcn_rcpf(1.0f + __expf(-1.702f * g));
;                         r[n * 4 + j] = (uu + 1.0f) * glu; }
;                 u32x2 w; w.x = pk4_fp8(r[0], r[1], r[2], r[3]); w.y = pk4_fp8(r[4], r[5], r[6], r[7]);
;                 *(u32x2*)(O + (size_t)(row0 + ai * HALF + m * 16) * DM + cc) = w; }
	v_mul_f32_e32 v26, v20, v26
	v_fmamk_f32 v20, v84, 0x3c800000, v4
	v_med3_f32 v20, v20, s57, v196
	v_mul_f32_e32 v27, v27, v28
	v_add_f32_e32 v20, 1.0, v20
	v_add_f32_e32 v28, 1.0, v30
	v_mul_f32_e32 v27, v20, v27
	v_fmamk_f32 v20, v85, 0x3c800000, v5
	v_rcp_f32_e32 v28, v28
	v_med3_f32 v30, v20, s57, v196
	v_mov_b32_e32 v20, v181
	v_cvt_pk_fp8_f32 v20, v21, v22
	v_mov_b32_e32 v21, v181
	v_cvt_pk_fp8_f32 v21, v25, v26
	v_mul_f32_e32 v28, v29, v28
	v_add_f32_e32 v22, 1.0, v30
	v_mul_f32_e32 v22, v22, v28
	v_cvt_pk_fp8_f32 v21, v27, v22 op_sel:[0,0,1]
	v_fmamk_f32 v22, v78, 0x3c800000, v14
	v_cvt_pk_fp8_f32 v20, v23, v24 op_sel:[0,0,1]
	v_min_f32_e32 v24, 0x40e00000, v22
	v_mul_f32_e32 v22, 0xbfd9db23, v24
	v_mul_f32_e32 v22, 0x3fb8aa3b, v22
	v_exp_f32_e32 v25, v22
	v_add_co_u32_e32 v22, vcc, s59, v18
	v_fmamk_f32 v27, v71, 0x3c800000, v7
	s_nop 0
	v_addc_co_u32_e32 v23, vcc, 0, v19, vcc
	global_store_dwordx2 v[22:23], v[20:21], off
	v_fmamk_f32 v22, v79, 0x3c800000, v15
	v_min_f32_e32 v22, 0x40e00000, v22
	v_mul_f32_e32 v23, 0xbfd9db23, v22
	v_mul_f32_e32 v23, 0x3fb8aa3b, v23
	v_exp_f32_e32 v23, v23
	v_add_f32_e32 v21, 1.0, v25
	v_rcp_f32_e32 v21, v21
	v_fmamk_f32 v25, v81, 0x3c800000, v17
	v_add_f32_e32 v23, 1.0, v23
	v_rcp_f32_e32 v23, v23
	v_mul_f32_e32 v21, v24, v21
	v_min_f32_e32 v25, 0x40e00000, v25
	v_mul_f32_e32 v26, 0xbfd9db23, v25
	v_mul_f32_e32 v22, v22, v23
	v_fmamk_f32 v23, v80, 0x3c800000, v16
	v_min_f32_e32 v23, 0x40e00000, v23
	v_mul_f32_e32 v24, 0xbfd9db23, v23
	v_mul_f32_e32 v24, 0x3fb8aa3b, v24
	v_exp_f32_e32 v24, v24
	v_mul_f32_e32 v26, 0x3fb8aa3b, v26
	v_exp_f32_e32 v26, v26
	v_min_f32_e32 v27, 0x40e00000, v27
	v_add_f32_e32 v24, 1.0, v24
	v_rcp_f32_e32 v24, v24
	v_mul_f32_e32 v28, 0xbfd9db23, v27
	v_mul_f32_e32 v28, 0x3fb8aa3b, v28
	v_exp_f32_e32 v28, v28
	v_mul_f32_e32 v23, v23, v24
	v_add_f32_e32 v24, 1.0, v26
	v_rcp_f32_e32 v24, v24
	v_fmamk_f32 v20, v74, 0x3c800000, v10
	v_med3_f32 v20, v20, s57, v196
	v_add_f32_e32 v20, 1.0, v20
	v_mul_f32_e32 v24, v25, v24
	v_fmamk_f32 v25, v70, 0x3c800000, v6
	v_min_f32_e32 v25, 0x40e00000, v25
	v_mul_f32_e32 v26, 0xbfd9db23, v25
	v_mul_f32_e32 v26, 0x3fb8aa3b, v26
	v_exp_f32_e32 v26, v26
	v_mul_f32_e32 v21, v20, v21
	v_fmamk_f32 v20, v75, 0x3c800000, v11
	v_med3_f32 v20, v20, s57, v196
	v_add_f32_e32 v26, 1.0, v26
	v_rcp_f32_e32 v26, v26
	v_add_f32_e32 v20, 1.0, v20
	v_mul_f32_e32 v22, v20, v22
	v_fmamk_f32 v20, v76, 0x3c800000, v12
	v_mul_f32_e32 v25, v25, v26
	v_add_f32_e32 v26, 1.0, v28
	v_rcp_f32_e32 v26, v26
	v_med3_f32 v20, v20, s57, v196
	v_add_f32_e32 v20, 1.0, v20
	v_mul_f32_e32 v23, v20, v23
	v_mul_f32_e32 v26, v27, v26
	v_fmamk_f32 v27, v72, 0x3c800000, v8
	v_min_f32_e32 v27, 0x40e00000, v27
	v_fmamk_f32 v20, v77, 0x3c800000, v13
	v_mul_f32_e32 v28, 0xbfd9db23, v27
	v_med3_f32 v20, v20, s57, v196
	v_mul_f32_e32 v28, 0x3fb8aa3b, v28
	v_add_f32_e32 v20, 1.0, v20
	v_exp_f32_e32 v28, v28
	v_mul_f32_e32 v24, v20, v24
	v_fmamk_f32 v20, v66, 0x3c800000, v2
	v_med3_f32 v20, v20, s57, v196
	v_fmamk_f32 v29, v73, 0x3c800000, v9
	v_add_f32_e32 v20, 1.0, v20
	v_min_f32_e32 v29, 0x40e00000, v29
	v_mul_f32_e32 v25, v20, v25
	v_fmamk_f32 v20, v67, 0x3c800000, v3
	v_add_f32_e32 v28, 1.0, v28
	v_mul_f32_e32 v30, 0xbfd9db23, v29
	v_med3_f32 v20, v20, s57, v196
	v_rcp_f32_e32 v28, v28
	v_mul_f32_e32 v30, 0x3fb8aa3b, v30
	v_add_f32_e32 v20, 1.0, v20
	v_exp_f32_e32 v30, v30
	v_mul_f32_e32 v26, v20, v26
	v_fmamk_f32 v20, v68, 0x3c800000, v4
	v_med3_f32 v20, v20, s57, v196
	v_mul_f32_e32 v27, v27, v28
	v_add_f32_e32 v20, 1.0, v20
	v_add_f32_e32 v28, 1.0, v30
	v_mul_f32_e32 v27, v20, v27
	v_fmamk_f32 v20, v69, 0x3c800000, v5
	v_rcp_f32_e32 v28, v28
	v_med3_f32 v30, v20, s57, v196
	v_mov_b32_e32 v20, v181
	v_cvt_pk_fp8_f32 v20, v21, v22
	v_mov_b32_e32 v21, v181
	v_cvt_pk_fp8_f32 v21, v25, v26
	v_mul_f32_e32 v28, v29, v28
	v_add_f32_e32 v22, 1.0, v30
	v_fmamk_f32 v14, v62, 0x3c800000, v14
	v_mul_f32_e32 v22, v22, v28
	v_min_f32_e32 v14, 0x40e00000, v14
	v_cvt_pk_fp8_f32 v21, v27, v22 op_sel:[0,0,1]
	v_mul_f32_e32 v22, 0xbfd9db23, v14
	v_cvt_pk_fp8_f32 v20, v23, v24 op_sel:[0,0,1]
	v_mul_f32_e32 v22, 0x3fb8aa3b, v22
	v_exp_f32_e32 v24, v22
	v_add_co_u32_e32 v22, vcc, s60, v18
	v_fmamk_f32 v15, v63, 0x3c800000, v15
	s_nop 0
	v_addc_co_u32_e32 v23, vcc, 0, v19, vcc
	v_min_f32_e32 v15, 0x40e00000, v15
	global_store_dwordx2 v[22:23], v[20:21], off
	v_mul_f32_e32 v21, 0xbfd9db23, v15
; __device__ __forceinline__ unsigned pk4_fp8(float a, float b, float c, float d) { int p = __builtin_amdgcn_cvt_pk_fp8_f32(a, b, 0, false); p = __builtin_amdgcn_cvt_pk_fp8_f32(c, d, p, true); return (unsigned)p; }
; __device__ __forceinline__ unsigned pk4_fp8_scaled(float a, float b, float c, float d) { s16x2 r = {0, 0}; r = __builtin_amdgcn_cvt_scalef32_pk_fp8_f32(r, a, b, pg8::W8_INV, false); r = __builtin_amdgcn_cvt_scalef32_pk_fp8_f32(r, c, d, pg8::W8_INV, true); return __builtin_bit_cast(unsigned, r); }
;     __device__ __forceinline__ void operator()(const f32x4 (&acc)[2][2][4][2], const Unit& u, int wr, int wc, int fr, int fq) const {
;     ...
;             for (int m = 0; m < 4; ++m) { float r[8];
; #pragma unroll
;                 for (int n = 0; n < 2; ++n)
; #pragma unroll
;                     for (int j = 0; j < 4; ++j) {
;                         float g = acc[ai][0][m][n][j] * W8_INV + bg[n][j], uu = acc[ai][1][m][n][j] * W8_INV + bu[n][j];
;                         g = fminf(g, 7.0f); uu = fminf(fmaxf(uu, -7.0f), 7.0f);
;                         const float glu = g * __builtin_amdgcn_rcpf(1.0f + __expf(-1.702f * g));
;                         r[n * 4 + j] = (uu + 1.0f) * glu; }
;                 u32x2 w; w.x = pk4_fp8(r[0], r[1], r[2], r[3]); w.y = pk4_fp8(r[4], r[5], r[6], r[7]);
;                 *(u32x2*)(O + (size_t)(row0 + ai * HALF + m * 16) * DM + cc) = w; }
; __device__ __forceinline__ void sjob_store(const SJob& c, const f32x4 (&v)[8]) {
; #pragma unroll
;     for (int jn = 0; jn < 4; ++jn) { u32x2 o;
;         o.x = pk4_fp8_scaled(v[0][jn], v[1][jn], v[2][jn], v[3][jn]); o.y = pk4_fp8_scaled(v[4][jn], v[5][jn], v[6][jn], v[7][jn]);
;         __builtin_nontemporal_store(o, (u32x2*)(c.dst + (size_t)jn * 2048)); }
; }
	v_add_f32_e32 v20, 1.0, v24
	v_mul_f32_e32 v21, 0x3fb8aa3b, v21
	v_rcp_f32_e32 v20, v20
	v_exp_f32_e32 v21, v21
	v_fmamk_f32 v10, v58, 0x3c800000, v10
	v_med3_f32 v10, v10, s57, v196
	v_mul_f32_e32 v14, v14, v20
	v_add_f32_e32 v20, 1.0, v21
	v_rcp_f32_e32 v20, v20
	v_add_f32_e32 v10, 1.0, v10
	v_mul_f32_e32 v10, v10, v14
	v_fmamk_f32 v11, v59, 0x3c800000, v11
	v_mul_f32_e32 v14, v15, v20
	v_fmamk_f32 v15, v64, 0x3c800000, v16
	v_min_f32_e32 v15, 0x40e00000, v15
	v_mul_f32_e32 v16, 0xbfd9db23, v15
	v_mul_f32_e32 v16, 0x3fb8aa3b, v16
	v_exp_f32_e32 v16, v16
	v_med3_f32 v11, v11, s57, v196
	v_add_f32_e32 v11, 1.0, v11
	v_fmac_f32_e32 v17, 0x3c800000, v65
	v_mul_f32_e32 v11, v11, v14
	v_add_f32_e32 v14, 1.0, v16
	v_min_f32_e32 v16, 0x40e00000, v17
	v_mul_f32_e32 v17, 0xbfd9db23, v16
	v_mul_f32_e32 v17, 0x3fb8aa3b, v17
	v_rcp_f32_e32 v14, v14
	v_exp_f32_e32 v17, v17
	v_fmamk_f32 v12, v60, 0x3c800000, v12
	v_med3_f32 v12, v12, s57, v196
	v_mul_f32_e32 v14, v15, v14
	v_add_f32_e32 v15, 1.0, v17
	v_rcp_f32_e32 v15, v15
	v_fmamk_f32 v6, v54, 0x3c800000, v6
	v_add_f32_e32 v12, 1.0, v12
	v_min_f32_e32 v6, 0x40e00000, v6
	v_mul_f32_e32 v12, v12, v14
	v_mul_f32_e32 v14, v16, v15
	v_mul_f32_e32 v15, 0xbfd9db23, v6
	v_mul_f32_e32 v15, 0x3fb8aa3b, v15
	v_exp_f32_e32 v15, v15
	v_fmac_f32_e32 v13, 0x3c800000, v61
	v_med3_f32 v13, v13, s57, v196
	v_fmamk_f32 v7, v55, 0x3c800000, v7
	v_add_f32_e32 v13, 1.0, v13
	v_min_f32_e32 v7, 0x40e00000, v7
	v_mul_f32_e32 v13, v13, v14
	v_add_f32_e32 v14, 1.0, v15
	v_mul_f32_e32 v15, 0xbfd9db23, v7
	v_mul_f32_e32 v15, 0x3fb8aa3b, v15
	v_rcp_f32_e32 v14, v14
	v_exp_f32_e32 v15, v15
	v_fmamk_f32 v2, v50, 0x3c800000, v2
	v_med3_f32 v2, v2, s57, v196
	v_mul_f32_e32 v6, v6, v14
	v_add_f32_e32 v14, 1.0, v15
	v_rcp_f32_e32 v14, v14
	v_add_f32_e32 v2, 1.0, v2
	v_mul_f32_e32 v6, v2, v6
	v_fmamk_f32 v2, v51, 0x3c800000, v3
	v_mul_f32_e32 v3, v7, v14
	v_fmamk_f32 v7, v56, 0x3c800000, v8
	v_min_f32_e32 v7, 0x40e00000, v7
	v_mul_f32_e32 v8, 0xbfd9db23, v7
	v_mul_f32_e32 v8, 0x3fb8aa3b, v8
	v_exp_f32_e32 v8, v8
	v_med3_f32 v2, v2, s57, v196
	v_add_f32_e32 v2, 1.0, v2
	v_fmac_f32_e32 v9, 0x3c800000, v57
	v_mul_f32_e32 v14, v2, v3
	v_fmamk_f32 v2, v52, 0x3c800000, v4
	v_min_f32_e32 v4, 0x40e00000, v9
	v_add_f32_e32 v3, 1.0, v8
	v_mul_f32_e32 v8, 0xbfd9db23, v4
	v_mul_f32_e32 v8, 0x3fb8aa3b, v8
	v_rcp_f32_e32 v3, v3
	v_exp_f32_e32 v8, v8
	v_med3_f32 v2, v2, s57, v196
	v_add_f32_e32 v2, 1.0, v2
	v_mul_f32_e32 v3, v7, v3
	v_add_f32_e32 v7, 1.0, v8
	v_rcp_f32_e32 v7, v7
	v_mul_f32_e32 v8, v2, v3
	v_mov_b32_e32 v2, v181
	v_mov_b32_e32 v3, v181
	v_fmac_f32_e32 v5, 0x3c800000, v53
	v_cvt_pk_fp8_f32 v2, v10, v11
	v_cvt_pk_fp8_f32 v3, v6, v14
	v_med3_f32 v5, v5, s57, v196
	v_mul_f32_e32 v4, v4, v7
	v_add_f32_e32 v5, 1.0, v5
	v_mul_f32_e32 v4, v5, v4
	v_cvt_pk_fp8_f32 v2, v12, v13 op_sel:[0,0,1]
	v_cvt_pk_fp8_f32 v3, v8, v4 op_sel:[0,0,1]
	v_add_co_u32_e32 v4, vcc, 0x58000, v18
	s_nop 1
	v_addc_co_u32_e32 v5, vcc, 0, v19, vcc
	s_and_b64 vcc, exec, s[22:23]
	global_store_dwordx2 v[4:5], v[2:3], off
	s_cmp_lg_u32 s82, 0
	s_cbranch_scc0 .Lesj_skip
	s_waitcnt vmcnt(8)
	v_cvt_scalef32_pk_fp8_f32 v250, v218, v222, v254
	v_cvt_scalef32_pk_fp8_f32 v251, v234, v238, v254
	v_cvt_scalef32_pk_fp8_f32 v250, v226, v230, v254 op_sel:[0,0,0,1]
	v_cvt_scalef32_pk_fp8_f32 v251, v242, v246, v254 op_sel:[0,0,0,1]
	global_store_dwordx2 v253, v[250:251], s[90:91] nt
	v_cvt_scalef32_pk_fp8_f32 v250, v219, v223, v254
	v_cvt_scalef32_pk_fp8_f32 v251, v235, v239, v254
	v_cvt_scalef32_pk_fp8_f32 v250, v227, v231, v254 op_sel:[0,0,0,1]
	v_cvt_scalef32_pk_fp8_f32 v251, v243, v247, v254 op_sel:[0,0,0,1]
	global_store_dwordx2 v253, v[250:251], s[90:91] offset:2048 nt
	v_cvt_scalef32_pk_fp8_f32 v250, v220, v224, v254
	v_cvt_scalef32_pk_fp8_f32 v251, v236, v240, v254
	v_cvt_scalef32_pk_fp8_f32 v250, v228, v232, v254 op_sel:[0,0,0,1]
	v_cvt_scalef32_pk_fp8_f32 v251, v244, v248, v254 op_sel:[0,0,0,1]
	s_add_u32 s90, s90, 0x1000
	s_addc_u32 s91, s91, 0
	global_store_dwordx2 v253, v[250:251], s[90:91] nt
	v_cvt_scalef32_pk_fp8_f32 v250, v221, v225, v254
	v_cvt_scalef32_pk_fp8_f32 v251, v237, v241, v254
	v_cvt_scalef32_pk_fp8_f32 v250, v229, v233, v254 op_sel:[0,0,0,1]
	v_cvt_scalef32_pk_fp8_f32 v251, v245, v249, v254 op_sel:[0,0,0,1]
	global_store_dwordx2 v253, v[250:251], s[90:91] offset:2048 nt
	s_add_i32 s98, s98, 1
.Lesj_skip:
	s_cbranch_vccnz .LBB0_871

; template <bool FP8, bool GATHER, class Epi, class Sched>
; __device__ __forceinline__ void gemm_phase(LAS unsigned char* lds, const Gemm g, const Sched& S, const Epi& E) {
;     ...
;         const bool has_next = S.next(ui + 1, nxt);
;         const bool cfull = FP8 ? true : (cur.full != 0);
;         nA = has_next ? (const char*)g.A + (size_t)nxt.pm * tstep : cA;
;         const char* nB = has_next ? (const char*)g.Bt + (size_t)nxt.e * estep + (size_t)nxt.pn * tstep : cB;
;     ...
; #pragma unroll
;         for (int a = 0; a < 2; ++a)
; #pragma unroll
;             for (int b = 0; b < 2; ++b)
; #pragma unroll
;                 for (int m = 0; m < 4; ++m)
; #pragma unroll
;                     for (int n = 0; n < 2; ++n) acc[a][b][m][n] = (f32x4){0.f, 0.f, 0.f, 0.f};
;         cur = nxt; cA = nA; cB = nB; ++ui;
.LBB0_864:
	s_ashr_i32 s17, s16, 31
	s_xor_b64 s[22:23], s[38:39], -1
	s_lshl_b64 s[20:21], s[16:17], 23
	s_add_u32 s2, s3, s20
	s_addc_u32 s17, s27, s21
	s_ashr_i32 s19, s18, 31
	s_lshl_b64 s[20:21], s[18:19], 19
	s_add_u32 s20, s2, s20
	s_addc_u32 s21, s17, s21
	s_and_b64 s[28:29], s[38:39], exec
	s_cselect_b32 s17, s21, s1
	s_cselect_b32 s19, s20, s0
	s_lshl_b32 s2, s80, 10
	s_add_u32 s25, s0, 0x100
	v_mov_b32_e32 v50, 0
	s_addc_u32 s28, s1, 0
	s_mov_b32 s29, -2
	v_add_u32_e32 v199, s2, v194
	v_mov_b32_e32 v51, v50
	v_mov_b32_e32 v52, v50
	v_mov_b32_e32 v53, v50
	v_mov_b32_e32 v58, v50
	v_mov_b32_e32 v59, v50
	v_mov_b32_e32 v60, v50
	v_mov_b32_e32 v61, v50
	v_mov_b32_e32 v66, v50
	v_mov_b32_e32 v67, v50
	v_mov_b32_e32 v68, v50
	v_mov_b32_e32 v69, v50
	v_mov_b32_e32 v74, v50
	v_mov_b32_e32 v75, v50
	v_mov_b32_e32 v76, v50
	v_mov_b32_e32 v77, v50
	v_mov_b32_e32 v82, v50
	v_mov_b32_e32 v83, v50
	v_mov_b32_e32 v84, v50
	v_mov_b32_e32 v85, v50
	v_mov_b32_e32 v90, v50
	v_mov_b32_e32 v91, v50
	v_mov_b32_e32 v92, v50
	v_mov_b32_e32 v93, v50
	v_mov_b32_e32 v98, v50
	v_mov_b32_e32 v99, v50
	v_mov_b32_e32 v100, v50
	v_mov_b32_e32 v101, v50
	v_mov_b32_e32 v106, v50
	v_mov_b32_e32 v107, v50
	v_mov_b32_e32 v108, v50
	v_mov_b32_e32 v109, v50
	v_mov_b32_e32 v54, v50
	v_mov_b32_e32 v55, v50
	v_mov_b32_e32 v56, v50
	v_mov_b32_e32 v57, v50
	v_mov_b32_e32 v62, v50
	v_mov_b32_e32 v63, v50
	v_mov_b32_e32 v64, v50
	v_mov_b32_e32 v65, v50
	v_mov_b32_e32 v70, v50
	v_mov_b32_e32 v71, v50
	v_mov_b32_e32 v72, v50
	v_mov_b32_e32 v73, v50
	v_mov_b32_e32 v78, v50
	v_mov_b32_e32 v79, v50
	v_mov_b32_e32 v80, v50
	v_mov_b32_e32 v81, v50
	v_mov_b32_e32 v86, v50
	v_mov_b32_e32 v87, v50
	v_mov_b32_e32 v88, v50
	v_mov_b32_e32 v89, v50
	v_mov_b32_e32 v94, v50
	v_mov_b32_e32 v95, v50
	v_mov_b32_e32 v96, v50
	v_mov_b32_e32 v97, v50
	v_mov_b32_e32 v102, v50
	v_mov_b32_e32 v103, v50
	v_mov_b32_e32 v104, v50
	v_mov_b32_e32 v105, v50
	v_mov_b32_e32 v110, v50
	v_mov_b32_e32 v111, v50
	v_mov_b32_e32 v112, v50
	v_mov_b32_e32 v113, v50
	v_mov_b32_e32 v114, v50
	v_mov_b32_e32 v115, v50
	v_mov_b32_e32 v116, v50
	v_mov_b32_e32 v117, v50
	v_mov_b32_e32 v122, v50
	v_mov_b32_e32 v123, v50
	v_mov_b32_e32 v124, v50
	v_mov_b32_e32 v125, v50
	v_mov_b32_e32 v130, v50
	v_mov_b32_e32 v131, v50
	v_mov_b32_e32 v132, v50
	v_mov_b32_e32 v133, v50
	v_mov_b32_e32 v138, v50
	v_mov_b32_e32 v139, v50
	v_mov_b32_e32 v140, v50
	v_mov_b32_e32 v141, v50
	v_mov_b32_e32 v146, v50
	v_mov_b32_e32 v147, v50
	v_mov_b32_e32 v148, v50
	v_mov_b32_e32 v149, v50
	v_mov_b32_e32 v154, v50
	v_mov_b32_e32 v155, v50
	v_mov_b32_e32 v156, v50
	v_mov_b32_e32 v157, v50
	v_mov_b32_e32 v162, v50
	v_mov_b32_e32 v163, v50
	v_mov_b32_e32 v164, v50
	v_mov_b32_e32 v165, v50
	v_mov_b32_e32 v170, v50
	v_mov_b32_e32 v171, v50
	v_mov_b32_e32 v172, v50
	v_mov_b32_e32 v173, v50
	v_mov_b32_e32 v118, v50
	v_mov_b32_e32 v119, v50
	v_mov_b32_e32 v120, v50
	v_mov_b32_e32 v121, v50
	v_mov_b32_e32 v126, v50
	v_mov_b32_e32 v127, v50
	v_mov_b32_e32 v128, v50
	v_mov_b32_e32 v129, v50
	v_mov_b32_e32 v134, v50
	v_mov_b32_e32 v135, v50
	v_mov_b32_e32 v136, v50
	v_mov_b32_e32 v137, v50
	v_mov_b32_e32 v142, v50
	v_mov_b32_e32 v143, v50
	v_mov_b32_e32 v144, v50
	v_mov_b32_e32 v145, v50
	v_mov_b32_e32 v150, v50
	v_mov_b32_e32 v151, v50
	v_mov_b32_e32 v152, v50
	v_mov_b32_e32 v153, v50
	v_mov_b32_e32 v158, v50
	v_mov_b32_e32 v159, v50
	v_mov_b32_e32 v160, v50
	v_mov_b32_e32 v161, v50
	v_mov_b32_e32 v166, v50
	v_mov_b32_e32 v167, v50
	v_mov_b32_e32 v168, v50
	v_mov_b32_e32 v169, v50
	v_mov_b32_e32 v174, v50
	v_mov_b32_e32 v175, v50
	v_mov_b32_e32 v176, v50
	v_mov_b32_e32 v177, v50
	s_add_i32 s32, s98, 7
	s_lshr_b32 s32, s32, 1
	s_mul_i32 s32, s32, s83
	s_add_i32 s32, s32, s84
	s_cmp_lt_u32 s32, 0x8000
	s_cselect_b32 s85, 1, 0
	s_cmp_lt_u32 s80, 2
	s_cselect_b32 s85, 0, s85
	s_cmp_gt_u32 s80, 4
	s_cselect_b32 s85, 0, s85
